# hand-written MoE weight conversion inside layer 0 attention phase (4 staggered workgroup groups at the unit loop header), units remapped across experts/k-blocks, packed output transposed through LDS s
# speedup vs baseline: 1.0261x; 1.0111x over previous
.LBB0_373:
	v_readlane_b32 s4, v255, 29
	v_readlane_b32 s5, v255, 5
	s_nop 4
	s_cmp_lg_u32 s4, s5
	s_cbranch_scc1 .Lcv_ret
	s_lshr_b32 s4, s19, 8
	s_bfe_u32 s5, s2, 0x20003
	s_cmp_lg_u32 s4, s5
	s_cbranch_scc1 .Lcv_ret
	s_branch .Lcv_body

.Lcv_body:
	v_readlane_b32 s40, v255, 5
	v_readlane_b32 s41, v255, 6
	v_mbcnt_lo_u32_b32 v4, -1, 0
	v_mbcnt_hi_u32_b32 v4, -1, v4
	s_nop 4
	s_load_dwordx2 s[34:35], s[40:41], 0x128
	v_lshlrev_b32_e32 v5, 2, v4
	s_mov_b32 s31, 0x7fffff
	s_lshr_b32 s29, s95, 6
	s_mov_b32 s22, 0
	s_lshl_b32 s32, s29, 14
	v_mul_u32_u24_e32 v12, 0x90, v4
	v_add_u32_e32 v12, s32, v12
	v_lshrrev_b32_e32 v13, 3, v4
	v_mul_u32_u24_e32 v13, 0x90, v13
	v_and_b32_e32 v7, 7, v4
	v_lshl_add_u32 v13, v7, 4, v13
	v_add_u32_e32 v13, s32, v13
	s_waitcnt lgkmcnt(0)
	s_barrier
.Lcv_unit:
	s_cmp_lt_u32 s22, 14
	s_cbranch_scc0 .Lcv_fp8
	s_lshl_b32 s23, s22, 8
	s_add_i32 s23, s23, s2
	s_cmp_ge_u32 s23, 0x700
	s_cselect_b32 s26, 1, 0
	s_mul_i32 s32, s26, 0x700
	s_sub_i32 s23, s23, s32
	s_and_b32 s25, s23, 15
	s_bfe_u32 s24, s23, 0x30004
	s_lshr_b32 s23, s23, 7
	s_lshl_b32 s23, s23, 3
	s_add_i32 s23, s23, s29
	s_lshl_b32 s32, s26, 3
	s_add_i32 s32, s32, 0x108
	s_load_dwordx2 s[6:7], s[40:41], s32
	s_mul_i32 s20, s24, 0x3800000
	s_mul_i32 s21, s25, 0x380000
	s_add_u32 s20, s20, s21
	s_lshl_b32 s21, s23, 8
	s_add_u32 s20, s20, s21
	s_mov_b32 s27, 0x7000
	s_waitcnt lgkmcnt(0)
	s_add_u32 s4, s6, s20
	s_addc_u32 s5, s7, 0
	s_mul_i32 s20, s24, 0x1c00000
	s_lshl_b32 s21, s25, 7
	s_add_u32 s20, s20, s21
	s_add_u32 s20, s20, 0x8400000
	s_add_u32 s10, s34, s20
	s_addc_u32 s11, s35, 0
	v_lshrrev_b32_e32 v9, 3, v4
	v_lshl_add_u32 v7, s23, 6, v9
	v_lshrrev_b32_e32 v8, 7, v7
	v_and_b32_e32 v9, 0x7f, v7
	v_lshl_add_u32 v8, v8, 8, v9
	s_lshl_b32 s32, s26, 7
	v_add_u32_e32 v8, s32, v8
	v_lshlrev_b32_e32 v6, 11, v8
	v_and_b32_e32 v9, 7, v4
	v_lshl_add_u32 v6, v9, 4, v6
	s_mov_b32 s32, 0x4000
	global_load_dword v40, v5, s[4:5] nt
	s_add_u32 s4, s4, s27
	s_addc_u32 s5, s5, 0
	global_load_dword v41, v5, s[4:5] nt
	s_add_u32 s4, s4, s27
	s_addc_u32 s5, s5, 0
	global_load_dword v42, v5, s[4:5] nt
	s_add_u32 s4, s4, s27
	s_addc_u32 s5, s5, 0
	global_load_dword v43, v5, s[4:5] nt
	s_add_u32 s4, s4, s27
	s_addc_u32 s5, s5, 0
	global_load_dword v44, v5, s[4:5] nt
	s_add_u32 s4, s4, s27
	s_addc_u32 s5, s5, 0
	global_load_dword v45, v5, s[4:5] nt
	s_add_u32 s4, s4, s27
	s_addc_u32 s5, s5, 0
	global_load_dword v46, v5, s[4:5] nt
	s_add_u32 s4, s4, s27
	s_addc_u32 s5, s5, 0
	global_load_dword v47, v5, s[4:5] nt
	s_add_u32 s4, s4, s27
	s_addc_u32 s5, s5, 0
	global_load_dword v48, v5, s[4:5] nt
	s_add_u32 s4, s4, s27
	s_addc_u32 s5, s5, 0
	global_load_dword v49, v5, s[4:5] nt
	s_add_u32 s4, s4, s27
	s_addc_u32 s5, s5, 0
	global_load_dword v50, v5, s[4:5] nt
	s_add_u32 s4, s4, s27
	s_addc_u32 s5, s5, 0
	global_load_dword v51, v5, s[4:5] nt
	s_add_u32 s4, s4, s27
	s_addc_u32 s5, s5, 0
	global_load_dword v52, v5, s[4:5] nt
	s_add_u32 s4, s4, s27
	s_addc_u32 s5, s5, 0
	global_load_dword v53, v5, s[4:5] nt
	s_add_u32 s4, s4, s27
	s_addc_u32 s5, s5, 0
	global_load_dword v54, v5, s[4:5] nt
	s_add_u32 s4, s4, s27
	s_addc_u32 s5, s5, 0
	global_load_dword v55, v5, s[4:5] nt
	s_add_u32 s4, s4, s27
	s_addc_u32 s5, s5, 0
	global_load_dword v56, v5, s[4:5] nt
	s_add_u32 s4, s4, s27
	s_addc_u32 s5, s5, 0
	global_load_dword v57, v5, s[4:5] nt
	s_add_u32 s4, s4, s27
	s_addc_u32 s5, s5, 0
	global_load_dword v58, v5, s[4:5] nt
	s_add_u32 s4, s4, s27
	s_addc_u32 s5, s5, 0
	global_load_dword v59, v5, s[4:5] nt
	s_add_u32 s4, s4, s27
	s_addc_u32 s5, s5, 0
	global_load_dword v60, v5, s[4:5] nt
	s_add_u32 s4, s4, s27
	s_addc_u32 s5, s5, 0
	global_load_dword v61, v5, s[4:5] nt
	s_add_u32 s4, s4, s27
	s_addc_u32 s5, s5, 0
	global_load_dword v62, v5, s[4:5] nt
	s_add_u32 s4, s4, s27
	s_addc_u32 s5, s5, 0
	global_load_dword v63, v5, s[4:5] nt
	s_add_u32 s4, s4, s27
	s_addc_u32 s5, s5, 0
	global_load_dword v64, v5, s[4:5] nt
	s_add_u32 s4, s4, s27
	s_addc_u32 s5, s5, 0
	global_load_dword v65, v5, s[4:5] nt
	s_add_u32 s4, s4, s27
	s_addc_u32 s5, s5, 0
	global_load_dword v66, v5, s[4:5] nt
	s_add_u32 s4, s4, s27
	s_addc_u32 s5, s5, 0
	global_load_dword v67, v5, s[4:5] nt
	s_add_u32 s4, s4, s27
	s_addc_u32 s5, s5, 0
	global_load_dword v68, v5, s[4:5] nt
	s_add_u32 s4, s4, s27
	s_addc_u32 s5, s5, 0
	global_load_dword v69, v5, s[4:5] nt
	s_add_u32 s4, s4, s27
	s_addc_u32 s5, s5, 0
	global_load_dword v70, v5, s[4:5] nt
	s_add_u32 s4, s4, s27
	s_addc_u32 s5, s5, 0
	global_load_dword v71, v5, s[4:5] nt
	s_add_u32 s4, s4, s27
	s_addc_u32 s5, s5, 0
	global_load_dword v72, v5, s[4:5] nt
	s_add_u32 s4, s4, s27
	s_addc_u32 s5, s5, 0
	global_load_dword v73, v5, s[4:5] nt
	s_add_u32 s4, s4, s27
	s_addc_u32 s5, s5, 0
	global_load_dword v74, v5, s[4:5] nt
	s_add_u32 s4, s4, s27
	s_addc_u32 s5, s5, 0
	global_load_dword v75, v5, s[4:5] nt
	s_add_u32 s4, s4, s27
	s_addc_u32 s5, s5, 0
	global_load_dword v76, v5, s[4:5] nt
	s_add_u32 s4, s4, s27
	s_addc_u32 s5, s5, 0
	global_load_dword v77, v5, s[4:5] nt
	s_add_u32 s4, s4, s27
	s_addc_u32 s5, s5, 0
	global_load_dword v78, v5, s[4:5] nt
	s_add_u32 s4, s4, s27
	s_addc_u32 s5, s5, 0
	global_load_dword v79, v5, s[4:5] nt
	s_add_u32 s4, s4, s27
	s_addc_u32 s5, s5, 0
	global_load_dword v80, v5, s[4:5] nt
	s_add_u32 s4, s4, s27
	s_addc_u32 s5, s5, 0
	global_load_dword v81, v5, s[4:5] nt
	s_add_u32 s4, s4, s27
	s_addc_u32 s5, s5, 0
	global_load_dword v82, v5, s[4:5] nt
	s_add_u32 s4, s4, s27
	s_addc_u32 s5, s5, 0
	global_load_dword v83, v5, s[4:5] nt
	s_add_u32 s4, s4, s27
	s_addc_u32 s5, s5, 0
	global_load_dword v84, v5, s[4:5] nt
	s_add_u32 s4, s4, s27
	s_addc_u32 s5, s5, 0
	global_load_dword v85, v5, s[4:5] nt
	s_add_u32 s4, s4, s27
	s_addc_u32 s5, s5, 0
	global_load_dword v86, v5, s[4:5] nt
	s_add_u32 s4, s4, s27
	s_addc_u32 s5, s5, 0
	global_load_dword v87, v5, s[4:5] nt
	s_add_u32 s4, s4, s27
	s_addc_u32 s5, s5, 0
	global_load_dword v88, v5, s[4:5] nt
	s_add_u32 s4, s4, s27
	s_addc_u32 s5, s5, 0
	global_load_dword v89, v5, s[4:5] nt
	s_add_u32 s4, s4, s27
	s_addc_u32 s5, s5, 0
	global_load_dword v90, v5, s[4:5] nt
	s_add_u32 s4, s4, s27
	s_addc_u32 s5, s5, 0
	global_load_dword v91, v5, s[4:5] nt
	s_add_u32 s4, s4, s27
	s_addc_u32 s5, s5, 0
	global_load_dword v92, v5, s[4:5] nt
	s_add_u32 s4, s4, s27
	s_addc_u32 s5, s5, 0
	global_load_dword v93, v5, s[4:5] nt
	s_add_u32 s4, s4, s27
	s_addc_u32 s5, s5, 0
	global_load_dword v94, v5, s[4:5] nt
	s_add_u32 s4, s4, s27
	s_addc_u32 s5, s5, 0
	global_load_dword v95, v5, s[4:5] nt
	s_add_u32 s4, s4, s27
	s_addc_u32 s5, s5, 0
	global_load_dword v96, v5, s[4:5] nt
	s_add_u32 s4, s4, s27
	s_addc_u32 s5, s5, 0
	global_load_dword v97, v5, s[4:5] nt
	s_add_u32 s4, s4, s27
	s_addc_u32 s5, s5, 0
	global_load_dword v98, v5, s[4:5] nt
	s_add_u32 s4, s4, s27
	s_addc_u32 s5, s5, 0
	global_load_dword v99, v5, s[4:5] nt
	s_add_u32 s4, s4, s27
	s_addc_u32 s5, s5, 0
	global_load_dword v100, v5, s[4:5] nt
	s_add_u32 s4, s4, s27
	s_addc_u32 s5, s5, 0
	global_load_dword v101, v5, s[4:5] nt
	s_add_u32 s4, s4, s27
	s_addc_u32 s5, s5, 0
	global_load_dword v102, v5, s[4:5] nt
	s_add_u32 s4, s4, s27
	s_addc_u32 s5, s5, 0
	global_load_dword v103, v5, s[4:5] nt
	s_add_u32 s4, s4, s27
	s_addc_u32 s5, s5, 0
	s_waitcnt vmcnt(32)
	v_max3_f32 v10, |v40|, |v41|, |v42|
	v_max3_f32 v10, v10, |v43|, |v44|
	v_max3_f32 v10, v10, |v45|, |v46|
	v_max3_f32 v10, v10, |v47|, |v48|
	v_max3_f32 v10, v10, |v49|, |v50|
	v_max3_f32 v10, v10, |v51|, |v52|
	v_max3_f32 v10, v10, |v53|, |v54|
	v_max3_f32 v10, v10, |v55|, |v56|
	v_max3_f32 v10, v10, |v57|, |v58|
	v_max3_f32 v10, v10, |v59|, |v60|
	v_max3_f32 v10, v10, |v61|, |v62|
	v_max3_f32 v10, v10, |v63|, |v64|
	v_max3_f32 v10, v10, |v65|, |v66|
	v_max3_f32 v10, v10, |v67|, |v68|
	v_max3_f32 v10, v10, |v69|, |v70|
	v_max_f32_e64 v10, v10, |v71|
	v_bfe_u32 v11, v10, 23, 8
	v_and_or_b32 v10, v10, s31, 0.5
	v_cmp_lt_f32_e32 vcc, 0x3f700000, v10
	s_nop 1
	v_addc_co_u32_e32 v11, vcc, 0, v11, vcc
	v_add_u32_e32 v11, 0xffffff7f, v11
	v_max_i32_e32 v11, 0xffffff82, v11
	v_add_u32_e32 v110, 0x7f, v11
	v_lshlrev_b32_e32 v11, 23, v110
	v_mov_b32_e32 v111, 0
	s_nop 0
	v_cvt_scalef32_2xpk16_fp6_f32 v[104:109], v[40:55], v[56:71], v11
	global_load_dword v40, v5, s[4:5] nt
	s_add_u32 s4, s4, s27
	s_addc_u32 s5, s5, 0
	global_load_dword v41, v5, s[4:5] nt
	s_add_u32 s4, s4, s27
	s_addc_u32 s5, s5, 0
	global_load_dword v42, v5, s[4:5] nt
	s_add_u32 s4, s4, s27
	s_addc_u32 s5, s5, 0
	global_load_dword v43, v5, s[4:5] nt
	s_add_u32 s4, s4, s27
	s_addc_u32 s5, s5, 0
	global_load_dword v44, v5, s[4:5] nt
	s_add_u32 s4, s4, s27
	s_addc_u32 s5, s5, 0
	global_load_dword v45, v5, s[4:5] nt
	s_add_u32 s4, s4, s27
	s_addc_u32 s5, s5, 0
	global_load_dword v46, v5, s[4:5] nt
	s_add_u32 s4, s4, s27
	s_addc_u32 s5, s5, 0
	global_load_dword v47, v5, s[4:5] nt
	s_add_u32 s4, s4, s27
	s_addc_u32 s5, s5, 0
	global_load_dword v48, v5, s[4:5] nt
	s_add_u32 s4, s4, s27
	s_addc_u32 s5, s5, 0
	global_load_dword v49, v5, s[4:5] nt
	s_add_u32 s4, s4, s27
	s_addc_u32 s5, s5, 0
	global_load_dword v50, v5, s[4:5] nt
	s_add_u32 s4, s4, s27
	s_addc_u32 s5, s5, 0
	global_load_dword v51, v5, s[4:5] nt
	s_add_u32 s4, s4, s27
	s_addc_u32 s5, s5, 0
	global_load_dword v52, v5, s[4:5] nt
	s_add_u32 s4, s4, s27
	s_addc_u32 s5, s5, 0
	global_load_dword v53, v5, s[4:5] nt
	s_add_u32 s4, s4, s27
	s_addc_u32 s5, s5, 0
	global_load_dword v54, v5, s[4:5] nt
	s_add_u32 s4, s4, s27
	s_addc_u32 s5, s5, 0
	global_load_dword v55, v5, s[4:5] nt
	s_add_u32 s4, s4, s27
	s_addc_u32 s5, s5, 0
	global_load_dword v56, v5, s[4:5] nt
	s_add_u32 s4, s4, s27
	s_addc_u32 s5, s5, 0
	global_load_dword v57, v5, s[4:5] nt
	s_add_u32 s4, s4, s27
	s_addc_u32 s5, s5, 0
	global_load_dword v58, v5, s[4:5] nt
	s_add_u32 s4, s4, s27
	s_addc_u32 s5, s5, 0
	global_load_dword v59, v5, s[4:5] nt
	s_add_u32 s4, s4, s27
	s_addc_u32 s5, s5, 0
	global_load_dword v60, v5, s[4:5] nt
	s_add_u32 s4, s4, s27
	s_addc_u32 s5, s5, 0
	global_load_dword v61, v5, s[4:5] nt
	s_add_u32 s4, s4, s27
	s_addc_u32 s5, s5, 0
	global_load_dword v62, v5, s[4:5] nt
	s_add_u32 s4, s4, s27
	s_addc_u32 s5, s5, 0
	global_load_dword v63, v5, s[4:5] nt
	s_add_u32 s4, s4, s27
	s_addc_u32 s5, s5, 0
	global_load_dword v64, v5, s[4:5] nt
	s_add_u32 s4, s4, s27
	s_addc_u32 s5, s5, 0
	global_load_dword v65, v5, s[4:5] nt
	s_add_u32 s4, s4, s27
	s_addc_u32 s5, s5, 0
	global_load_dword v66, v5, s[4:5] nt
	s_add_u32 s4, s4, s27
	s_addc_u32 s5, s5, 0
	global_load_dword v67, v5, s[4:5] nt
	s_add_u32 s4, s4, s27
	s_addc_u32 s5, s5, 0
	global_load_dword v68, v5, s[4:5] nt
	s_add_u32 s4, s4, s27
	s_addc_u32 s5, s5, 0
	global_load_dword v69, v5, s[4:5] nt
	s_add_u32 s4, s4, s27
	s_addc_u32 s5, s5, 0
	global_load_dword v70, v5, s[4:5] nt
	s_add_u32 s4, s4, s27
	s_addc_u32 s5, s5, 0
	global_load_dword v71, v5, s[4:5] nt
	s_add_u32 s4, s4, s27
	s_addc_u32 s5, s5, 0
	s_waitcnt vmcnt(32)
	v_max3_f32 v10, |v72|, |v73|, |v74|
	v_max3_f32 v10, v10, |v75|, |v76|
	v_max3_f32 v10, v10, |v77|, |v78|
	v_max3_f32 v10, v10, |v79|, |v80|
	v_max3_f32 v10, v10, |v81|, |v82|
	v_max3_f32 v10, v10, |v83|, |v84|
	v_max3_f32 v10, v10, |v85|, |v86|
	v_max3_f32 v10, v10, |v87|, |v88|
	v_max3_f32 v10, v10, |v89|, |v90|
	v_max3_f32 v10, v10, |v91|, |v92|
	v_max3_f32 v10, v10, |v93|, |v94|
	v_max3_f32 v10, v10, |v95|, |v96|
	v_max3_f32 v10, v10, |v97|, |v98|
	v_max3_f32 v10, v10, |v99|, |v100|
	v_max3_f32 v10, v10, |v101|, |v102|
	v_max_f32_e64 v10, v10, |v103|
	v_bfe_u32 v11, v10, 23, 8
	v_and_or_b32 v10, v10, s31, 0.5
	v_cmp_lt_f32_e32 vcc, 0x3f700000, v10
	s_nop 1
	v_addc_co_u32_e32 v11, vcc, 0, v11, vcc
	v_add_u32_e32 v11, 0xffffff7f, v11
	v_max_i32_e32 v11, 0xffffff82, v11
	v_add_u32_e32 v118, 0x7f, v11
	v_lshlrev_b32_e32 v11, 23, v118
	v_mov_b32_e32 v119, 0
	s_nop 0
	v_cvt_scalef32_2xpk16_fp6_f32 v[112:117], v[72:87], v[88:103], v11
	global_load_dword v72, v5, s[4:5] nt
	s_add_u32 s4, s4, s27
	s_addc_u32 s5, s5, 0
	global_load_dword v73, v5, s[4:5] nt
	s_add_u32 s4, s4, s27
	s_addc_u32 s5, s5, 0
	global_load_dword v74, v5, s[4:5] nt
	s_add_u32 s4, s4, s27
	s_addc_u32 s5, s5, 0
	global_load_dword v75, v5, s[4:5] nt
	s_add_u32 s4, s4, s27
	s_addc_u32 s5, s5, 0
	global_load_dword v76, v5, s[4:5] nt
	s_add_u32 s4, s4, s27
	s_addc_u32 s5, s5, 0
	global_load_dword v77, v5, s[4:5] nt
	s_add_u32 s4, s4, s27
	s_addc_u32 s5, s5, 0
	global_load_dword v78, v5, s[4:5] nt
	s_add_u32 s4, s4, s27
	s_addc_u32 s5, s5, 0
	global_load_dword v79, v5, s[4:5] nt
	s_add_u32 s4, s4, s27
	s_addc_u32 s5, s5, 0
	global_load_dword v80, v5, s[4:5] nt
	s_add_u32 s4, s4, s27
	s_addc_u32 s5, s5, 0
	global_load_dword v81, v5, s[4:5] nt
	s_add_u32 s4, s4, s27
	s_addc_u32 s5, s5, 0
	global_load_dword v82, v5, s[4:5] nt
	s_add_u32 s4, s4, s27
	s_addc_u32 s5, s5, 0
	global_load_dword v83, v5, s[4:5] nt
	s_add_u32 s4, s4, s27
	s_addc_u32 s5, s5, 0
	global_load_dword v84, v5, s[4:5] nt
	s_add_u32 s4, s4, s27
	s_addc_u32 s5, s5, 0
	global_load_dword v85, v5, s[4:5] nt
	s_add_u32 s4, s4, s27
	s_addc_u32 s5, s5, 0
	global_load_dword v86, v5, s[4:5] nt
	s_add_u32 s4, s4, s27
	s_addc_u32 s5, s5, 0
	global_load_dword v87, v5, s[4:5] nt
	s_add_u32 s4, s4, s27
	s_addc_u32 s5, s5, 0
	global_load_dword v88, v5, s[4:5] nt
	s_add_u32 s4, s4, s27
	s_addc_u32 s5, s5, 0
	global_load_dword v89, v5, s[4:5] nt
	s_add_u32 s4, s4, s27
	s_addc_u32 s5, s5, 0
	global_load_dword v90, v5, s[4:5] nt
	s_add_u32 s4, s4, s27
	s_addc_u32 s5, s5, 0
	global_load_dword v91, v5, s[4:5] nt
	s_add_u32 s4, s4, s27
	s_addc_u32 s5, s5, 0
	global_load_dword v92, v5, s[4:5] nt
	s_add_u32 s4, s4, s27
	s_addc_u32 s5, s5, 0
	global_load_dword v93, v5, s[4:5] nt
	s_add_u32 s4, s4, s27
	s_addc_u32 s5, s5, 0
	global_load_dword v94, v5, s[4:5] nt
	s_add_u32 s4, s4, s27
	s_addc_u32 s5, s5, 0
	global_load_dword v95, v5, s[4:5] nt
	s_add_u32 s4, s4, s27
	s_addc_u32 s5, s5, 0
	global_load_dword v96, v5, s[4:5] nt
	s_add_u32 s4, s4, s27
	s_addc_u32 s5, s5, 0
	global_load_dword v97, v5, s[4:5] nt
	s_add_u32 s4, s4, s27
	s_addc_u32 s5, s5, 0
	global_load_dword v98, v5, s[4:5] nt
	s_add_u32 s4, s4, s27
	s_addc_u32 s5, s5, 0
	global_load_dword v99, v5, s[4:5] nt
	s_add_u32 s4, s4, s27
	s_addc_u32 s5, s5, 0
	global_load_dword v100, v5, s[4:5] nt
	s_add_u32 s4, s4, s27
	s_addc_u32 s5, s5, 0
	global_load_dword v101, v5, s[4:5] nt
	s_add_u32 s4, s4, s27
	s_addc_u32 s5, s5, 0
	global_load_dword v102, v5, s[4:5] nt
	s_add_u32 s4, s4, s27
	s_addc_u32 s5, s5, 0
	global_load_dword v103, v5, s[4:5] nt
	s_add_u32 s4, s4, s27
	s_addc_u32 s5, s5, 0
	s_waitcnt vmcnt(32)
	v_max3_f32 v10, |v40|, |v41|, |v42|
	v_max3_f32 v10, v10, |v43|, |v44|
	v_max3_f32 v10, v10, |v45|, |v46|
	v_max3_f32 v10, v10, |v47|, |v48|
	v_max3_f32 v10, v10, |v49|, |v50|
	v_max3_f32 v10, v10, |v51|, |v52|
	v_max3_f32 v10, v10, |v53|, |v54|
	v_max3_f32 v10, v10, |v55|, |v56|
	v_max3_f32 v10, v10, |v57|, |v58|
	v_max3_f32 v10, v10, |v59|, |v60|
	v_max3_f32 v10, v10, |v61|, |v62|
	v_max3_f32 v10, v10, |v63|, |v64|
	v_max3_f32 v10, v10, |v65|, |v66|
	v_max3_f32 v10, v10, |v67|, |v68|
	v_max3_f32 v10, v10, |v69|, |v70|
	v_max_f32_e64 v10, v10, |v71|
	v_bfe_u32 v11, v10, 23, 8
	v_and_or_b32 v10, v10, s31, 0.5
	v_cmp_lt_f32_e32 vcc, 0x3f700000, v10
	s_nop 1
	v_addc_co_u32_e32 v11, vcc, 0, v11, vcc
	v_add_u32_e32 v11, 0xffffff7f, v11
	v_max_i32_e32 v11, 0xffffff82, v11
	v_add_u32_e32 v126, 0x7f, v11
	v_lshlrev_b32_e32 v11, 23, v126
	v_mov_b32_e32 v127, 0
	s_nop 0
	v_cvt_scalef32_2xpk16_fp6_f32 v[120:125], v[40:55], v[56:71], v11
	s_waitcnt vmcnt(0)
	v_max3_f32 v10, |v72|, |v73|, |v74|
	v_max3_f32 v10, v10, |v75|, |v76|
	v_max3_f32 v10, v10, |v77|, |v78|
	v_max3_f32 v10, v10, |v79|, |v80|
	v_max3_f32 v10, v10, |v81|, |v82|
	v_max3_f32 v10, v10, |v83|, |v84|
	v_max3_f32 v10, v10, |v85|, |v86|
	v_max3_f32 v10, v10, |v87|, |v88|
	v_max3_f32 v10, v10, |v89|, |v90|
	v_max3_f32 v10, v10, |v91|, |v92|
	v_max3_f32 v10, v10, |v93|, |v94|
	v_max3_f32 v10, v10, |v95|, |v96|
	v_max3_f32 v10, v10, |v97|, |v98|
	v_max3_f32 v10, v10, |v99|, |v100|
	v_max3_f32 v10, v10, |v101|, |v102|
	v_max_f32_e64 v10, v10, |v103|
	v_bfe_u32 v11, v10, 23, 8
	v_and_or_b32 v10, v10, s31, 0.5
	v_cmp_lt_f32_e32 vcc, 0x3f700000, v10
	s_nop 1
	v_addc_co_u32_e32 v11, vcc, 0, v11, vcc
	v_add_u32_e32 v11, 0xffffff7f, v11
	v_max_i32_e32 v11, 0xffffff82, v11
	v_add_u32_e32 v134, 0x7f, v11
	v_lshlrev_b32_e32 v11, 23, v134
	v_mov_b32_e32 v135, 0
	s_nop 0
	v_cvt_scalef32_2xpk16_fp6_f32 v[128:133], v[72:87], v[88:103], v11
	s_nop 4
	ds_write_b128 v12, v[104:107]
	ds_write_b128 v12, v[112:115] offset:16
	ds_write_b128 v12, v[120:123] offset:32
	ds_write_b128 v12, v[128:131] offset:48
	ds_write_b128 v12, v[108:111] offset:64
	ds_write_b128 v12, v[116:119] offset:80
	ds_write_b128 v12, v[124:127] offset:96
	ds_write_b128 v12, v[132:135] offset:112
	ds_read_b128 v[40:43], v13
	ds_read_b128 v[44:47], v13 offset:1152
	ds_read_b128 v[48:51], v13 offset:2304
	ds_read_b128 v[52:55], v13 offset:3456
	ds_read_b128 v[56:59], v13 offset:4608
	ds_read_b128 v[60:63], v13 offset:5760
	ds_read_b128 v[64:67], v13 offset:6912
	ds_read_b128 v[68:71], v13 offset:8064
	s_waitcnt lgkmcnt(7)
	global_store_dwordx4 v6, v[40:43], s[10:11]
	v_add_u32_e32 v6, s32, v6
	s_waitcnt lgkmcnt(6)
	global_store_dwordx4 v6, v[44:47], s[10:11]
	v_add_u32_e32 v6, s32, v6
	s_waitcnt lgkmcnt(5)
	global_store_dwordx4 v6, v[48:51], s[10:11]
	v_add_u32_e32 v6, s32, v6
	s_waitcnt lgkmcnt(4)
	global_store_dwordx4 v6, v[52:55], s[10:11]
	v_add_u32_e32 v6, s32, v6
	s_waitcnt lgkmcnt(3)
	global_store_dwordx4 v6, v[56:59], s[10:11]
	v_add_u32_e32 v6, s32, v6
	s_waitcnt lgkmcnt(2)
	global_store_dwordx4 v6, v[60:63], s[10:11]
	v_add_u32_e32 v6, s32, v6
	s_waitcnt lgkmcnt(1)
	global_store_dwordx4 v6, v[64:67], s[10:11]
	v_add_u32_e32 v6, s32, v6
	s_waitcnt lgkmcnt(0)
	global_store_dwordx4 v6, v[68:71], s[10:11]
	s_branch .Lcv_next
.Lcv_fp8:
	s_sub_i32 s23, s22, 14
	s_lshl_b32 s23, s23, 8
	s_add_i32 s23, s23, s2
	s_and_b32 s24, s23, 7
	s_lshr_b32 s25, s23, 3
	s_mul_i32 s32, s25, 293
	s_lshr_b32 s32, s32, 14
	s_mul_i32 s23, s32, 56
	s_sub_i32 s25, s25, s23
	s_lshl_b32 s23, s32, 3
	s_add_i32 s23, s23, s29
	s_load_dwordx2 s[6:7], s[40:41], 0x118
	s_mul_i32 s20, s24, 0x3800000
	s_lshl_b32 s21, s25, 20
	s_add_u32 s20, s20, s21
	s_lshl_b32 s21, s23, 8
	s_add_u32 s20, s20, s21
	s_mov_b32 s27, 0x2000
	s_waitcnt lgkmcnt(0)
	s_add_u32 s4, s6, s20
	s_addc_u32 s5, s7, 0
	s_mul_i32 s20, s24, 0xe00000
	s_lshl_b32 s21, s25, 7
	s_add_u32 s20, s20, s21
	s_add_u32 s20, s20, 0x24400000
	s_add_u32 s10, s34, s20
	s_addc_u32 s11, s35, 0
	v_lshrrev_b32_e32 v9, 3, v4
	v_lshl_add_u32 v7, s23, 6, v9
	v_mul_u32_u24_e32 v6, 0x1c00, v7
	v_and_b32_e32 v9, 7, v4
	v_lshl_add_u32 v6, v9, 4, v6
	s_mov_b32 s32, 0xe000
	global_load_dword v40, v5, s[4:5] nt
	s_add_u32 s4, s4, s27
	s_addc_u32 s5, s5, 0
	global_load_dword v41, v5, s[4:5] nt
	s_add_u32 s4, s4, s27
	s_addc_u32 s5, s5, 0
	global_load_dword v42, v5, s[4:5] nt
	s_add_u32 s4, s4, s27
	s_addc_u32 s5, s5, 0
	global_load_dword v43, v5, s[4:5] nt
	s_add_u32 s4, s4, s27
	s_addc_u32 s5, s5, 0
	global_load_dword v44, v5, s[4:5] nt
	s_add_u32 s4, s4, s27
	s_addc_u32 s5, s5, 0
	global_load_dword v45, v5, s[4:5] nt
	s_add_u32 s4, s4, s27
	s_addc_u32 s5, s5, 0
	global_load_dword v46, v5, s[4:5] nt
	s_add_u32 s4, s4, s27
	s_addc_u32 s5, s5, 0
	global_load_dword v47, v5, s[4:5] nt
	s_add_u32 s4, s4, s27
	s_addc_u32 s5, s5, 0
	global_load_dword v48, v5, s[4:5] nt
	s_add_u32 s4, s4, s27
	s_addc_u32 s5, s5, 0
	global_load_dword v49, v5, s[4:5] nt
	s_add_u32 s4, s4, s27
	s_addc_u32 s5, s5, 0
	global_load_dword v50, v5, s[4:5] nt
	s_add_u32 s4, s4, s27
	s_addc_u32 s5, s5, 0
	global_load_dword v51, v5, s[4:5] nt
	s_add_u32 s4, s4, s27
	s_addc_u32 s5, s5, 0
	global_load_dword v52, v5, s[4:5] nt
	s_add_u32 s4, s4, s27
	s_addc_u32 s5, s5, 0
	global_load_dword v53, v5, s[4:5] nt
	s_add_u32 s4, s4, s27
	s_addc_u32 s5, s5, 0
	global_load_dword v54, v5, s[4:5] nt
	s_add_u32 s4, s4, s27
	s_addc_u32 s5, s5, 0
	global_load_dword v55, v5, s[4:5] nt
	s_add_u32 s4, s4, s27
	s_addc_u32 s5, s5, 0
	global_load_dword v56, v5, s[4:5] nt
	s_add_u32 s4, s4, s27
	s_addc_u32 s5, s5, 0
	global_load_dword v57, v5, s[4:5] nt
	s_add_u32 s4, s4, s27
	s_addc_u32 s5, s5, 0
	global_load_dword v58, v5, s[4:5] nt
	s_add_u32 s4, s4, s27
	s_addc_u32 s5, s5, 0
	global_load_dword v59, v5, s[4:5] nt
	s_add_u32 s4, s4, s27
	s_addc_u32 s5, s5, 0
	global_load_dword v60, v5, s[4:5] nt
	s_add_u32 s4, s4, s27
	s_addc_u32 s5, s5, 0
	global_load_dword v61, v5, s[4:5] nt
	s_add_u32 s4, s4, s27
	s_addc_u32 s5, s5, 0
	global_load_dword v62, v5, s[4:5] nt
	s_add_u32 s4, s4, s27
	s_addc_u32 s5, s5, 0
	global_load_dword v63, v5, s[4:5] nt
	s_add_u32 s4, s4, s27
	s_addc_u32 s5, s5, 0
	global_load_dword v64, v5, s[4:5] nt
	s_add_u32 s4, s4, s27
	s_addc_u32 s5, s5, 0
	global_load_dword v65, v5, s[4:5] nt
	s_add_u32 s4, s4, s27
	s_addc_u32 s5, s5, 0
	global_load_dword v66, v5, s[4:5] nt
	s_add_u32 s4, s4, s27
	s_addc_u32 s5, s5, 0
	global_load_dword v67, v5, s[4:5] nt
	s_add_u32 s4, s4, s27
	s_addc_u32 s5, s5, 0
	global_load_dword v68, v5, s[4:5] nt
	s_add_u32 s4, s4, s27
	s_addc_u32 s5, s5, 0
	global_load_dword v69, v5, s[4:5] nt
	s_add_u32 s4, s4, s27
	s_addc_u32 s5, s5, 0
	global_load_dword v70, v5, s[4:5] nt
	s_add_u32 s4, s4, s27
	s_addc_u32 s5, s5, 0
	global_load_dword v71, v5, s[4:5] nt
	s_add_u32 s4, s4, s27
	s_addc_u32 s5, s5, 0
	global_load_dword v72, v5, s[4:5] nt
	s_add_u32 s4, s4, s27
	s_addc_u32 s5, s5, 0
	global_load_dword v73, v5, s[4:5] nt
	s_add_u32 s4, s4, s27
	s_addc_u32 s5, s5, 0
	global_load_dword v74, v5, s[4:5] nt
	s_add_u32 s4, s4, s27
	s_addc_u32 s5, s5, 0
	global_load_dword v75, v5, s[4:5] nt
	s_add_u32 s4, s4, s27
	s_addc_u32 s5, s5, 0
	global_load_dword v76, v5, s[4:5] nt
	s_add_u32 s4, s4, s27
	s_addc_u32 s5, s5, 0
	global_load_dword v77, v5, s[4:5] nt
	s_add_u32 s4, s4, s27
	s_addc_u32 s5, s5, 0
	global_load_dword v78, v5, s[4:5] nt
	s_add_u32 s4, s4, s27
	s_addc_u32 s5, s5, 0
	global_load_dword v79, v5, s[4:5] nt
	s_add_u32 s4, s4, s27
	s_addc_u32 s5, s5, 0
	global_load_dword v80, v5, s[4:5] nt
	s_add_u32 s4, s4, s27
	s_addc_u32 s5, s5, 0
	global_load_dword v81, v5, s[4:5] nt
	s_add_u32 s4, s4, s27
	s_addc_u32 s5, s5, 0
	global_load_dword v82, v5, s[4:5] nt
	s_add_u32 s4, s4, s27
	s_addc_u32 s5, s5, 0
	global_load_dword v83, v5, s[4:5] nt
	s_add_u32 s4, s4, s27
	s_addc_u32 s5, s5, 0
	global_load_dword v84, v5, s[4:5] nt
	s_add_u32 s4, s4, s27
	s_addc_u32 s5, s5, 0
	global_load_dword v85, v5, s[4:5] nt
	s_add_u32 s4, s4, s27
	s_addc_u32 s5, s5, 0
	global_load_dword v86, v5, s[4:5] nt
	s_add_u32 s4, s4, s27
	s_addc_u32 s5, s5, 0
	global_load_dword v87, v5, s[4:5] nt
	s_add_u32 s4, s4, s27
	s_addc_u32 s5, s5, 0
	global_load_dword v88, v5, s[4:5] nt
	s_add_u32 s4, s4, s27
	s_addc_u32 s5, s5, 0
	global_load_dword v89, v5, s[4:5] nt
	s_add_u32 s4, s4, s27
	s_addc_u32 s5, s5, 0
	global_load_dword v90, v5, s[4:5] nt
	s_add_u32 s4, s4, s27
	s_addc_u32 s5, s5, 0
	global_load_dword v91, v5, s[4:5] nt
	s_add_u32 s4, s4, s27
	s_addc_u32 s5, s5, 0
	global_load_dword v92, v5, s[4:5] nt
	s_add_u32 s4, s4, s27
	s_addc_u32 s5, s5, 0
	global_load_dword v93, v5, s[4:5] nt
	s_add_u32 s4, s4, s27
	s_addc_u32 s5, s5, 0
	global_load_dword v94, v5, s[4:5] nt
	s_add_u32 s4, s4, s27
	s_addc_u32 s5, s5, 0
	global_load_dword v95, v5, s[4:5] nt
	s_add_u32 s4, s4, s27
	s_addc_u32 s5, s5, 0
	global_load_dword v96, v5, s[4:5] nt
	s_add_u32 s4, s4, s27
	s_addc_u32 s5, s5, 0
	global_load_dword v97, v5, s[4:5] nt
	s_add_u32 s4, s4, s27
	s_addc_u32 s5, s5, 0
	global_load_dword v98, v5, s[4:5] nt
	s_add_u32 s4, s4, s27
	s_addc_u32 s5, s5, 0
	global_load_dword v99, v5, s[4:5] nt
	s_add_u32 s4, s4, s27
	s_addc_u32 s5, s5, 0
	global_load_dword v100, v5, s[4:5] nt
	s_add_u32 s4, s4, s27
	s_addc_u32 s5, s5, 0
	global_load_dword v101, v5, s[4:5] nt
	s_add_u32 s4, s4, s27
	s_addc_u32 s5, s5, 0
	global_load_dword v102, v5, s[4:5] nt
	s_add_u32 s4, s4, s27
	s_addc_u32 s5, s5, 0
	global_load_dword v103, v5, s[4:5] nt
	s_add_u32 s4, s4, s27
	s_addc_u32 s5, s5, 0
	s_waitcnt vmcnt(32)
	v_mul_f32_e32 v40, 0x42800000, v40
	v_mul_f32_e32 v41, 0x42800000, v41
	v_mul_f32_e32 v42, 0x42800000, v42
	v_mul_f32_e32 v43, 0x42800000, v43
	v_mul_f32_e32 v44, 0x42800000, v44
	v_mul_f32_e32 v45, 0x42800000, v45
	v_mul_f32_e32 v46, 0x42800000, v46
	v_mul_f32_e32 v47, 0x42800000, v47
	v_mul_f32_e32 v48, 0x42800000, v48
	v_mul_f32_e32 v49, 0x42800000, v49
	v_mul_f32_e32 v50, 0x42800000, v50
	v_mul_f32_e32 v51, 0x42800000, v51
	v_mul_f32_e32 v52, 0x42800000, v52
	v_mul_f32_e32 v53, 0x42800000, v53
	v_mul_f32_e32 v54, 0x42800000, v54
	v_mul_f32_e32 v55, 0x42800000, v55
	v_mul_f32_e32 v56, 0x42800000, v56
	v_mul_f32_e32 v57, 0x42800000, v57
	v_mul_f32_e32 v58, 0x42800000, v58
	v_mul_f32_e32 v59, 0x42800000, v59
	v_mul_f32_e32 v60, 0x42800000, v60
	v_mul_f32_e32 v61, 0x42800000, v61
	v_mul_f32_e32 v62, 0x42800000, v62
	v_mul_f32_e32 v63, 0x42800000, v63
	v_mul_f32_e32 v64, 0x42800000, v64
	v_mul_f32_e32 v65, 0x42800000, v65
	v_mul_f32_e32 v66, 0x42800000, v66
	v_mul_f32_e32 v67, 0x42800000, v67
	v_mul_f32_e32 v68, 0x42800000, v68
	v_mul_f32_e32 v69, 0x42800000, v69
	v_mul_f32_e32 v70, 0x42800000, v70
	v_mul_f32_e32 v71, 0x42800000, v71
	v_cvt_pk_fp8_f32 v104, v40, v41
	v_cvt_pk_fp8_f32 v104, v42, v43 op_sel:[0,0,1]
	v_cvt_pk_fp8_f32 v105, v44, v45
	v_cvt_pk_fp8_f32 v105, v46, v47 op_sel:[0,0,1]
	v_cvt_pk_fp8_f32 v106, v48, v49
	v_cvt_pk_fp8_f32 v106, v50, v51 op_sel:[0,0,1]
	v_cvt_pk_fp8_f32 v107, v52, v53
	v_cvt_pk_fp8_f32 v107, v54, v55 op_sel:[0,0,1]
	v_cvt_pk_fp8_f32 v108, v56, v57
	v_cvt_pk_fp8_f32 v108, v58, v59 op_sel:[0,0,1]
	v_cvt_pk_fp8_f32 v109, v60, v61
	v_cvt_pk_fp8_f32 v109, v62, v63 op_sel:[0,0,1]
	v_cvt_pk_fp8_f32 v110, v64, v65
	v_cvt_pk_fp8_f32 v110, v66, v67 op_sel:[0,0,1]
	v_cvt_pk_fp8_f32 v111, v68, v69
	v_cvt_pk_fp8_f32 v111, v70, v71 op_sel:[0,0,1]
	global_load_dword v40, v5, s[4:5] nt
	s_add_u32 s4, s4, s27
	s_addc_u32 s5, s5, 0
	global_load_dword v41, v5, s[4:5] nt
	s_add_u32 s4, s4, s27
	s_addc_u32 s5, s5, 0
	global_load_dword v42, v5, s[4:5] nt
	s_add_u32 s4, s4, s27
	s_addc_u32 s5, s5, 0
	global_load_dword v43, v5, s[4:5] nt
	s_add_u32 s4, s4, s27
	s_addc_u32 s5, s5, 0
	global_load_dword v44, v5, s[4:5] nt
	s_add_u32 s4, s4, s27
	s_addc_u32 s5, s5, 0
	global_load_dword v45, v5, s[4:5] nt
	s_add_u32 s4, s4, s27
	s_addc_u32 s5, s5, 0
	global_load_dword v46, v5, s[4:5] nt
	s_add_u32 s4, s4, s27
	s_addc_u32 s5, s5, 0
	global_load_dword v47, v5, s[4:5] nt
	s_add_u32 s4, s4, s27
	s_addc_u32 s5, s5, 0
	global_load_dword v48, v5, s[4:5] nt
	s_add_u32 s4, s4, s27
	s_addc_u32 s5, s5, 0
	global_load_dword v49, v5, s[4:5] nt
	s_add_u32 s4, s4, s27
	s_addc_u32 s5, s5, 0
	global_load_dword v50, v5, s[4:5] nt
	s_add_u32 s4, s4, s27
	s_addc_u32 s5, s5, 0
	global_load_dword v51, v5, s[4:5] nt
	s_add_u32 s4, s4, s27
	s_addc_u32 s5, s5, 0
	global_load_dword v52, v5, s[4:5] nt
	s_add_u32 s4, s4, s27
	s_addc_u32 s5, s5, 0
	global_load_dword v53, v5, s[4:5] nt
	s_add_u32 s4, s4, s27
	s_addc_u32 s5, s5, 0
	global_load_dword v54, v5, s[4:5] nt
	s_add_u32 s4, s4, s27
	s_addc_u32 s5, s5, 0
	global_load_dword v55, v5, s[4:5] nt
	s_add_u32 s4, s4, s27
	s_addc_u32 s5, s5, 0
	global_load_dword v56, v5, s[4:5] nt
	s_add_u32 s4, s4, s27
	s_addc_u32 s5, s5, 0
	global_load_dword v57, v5, s[4:5] nt
	s_add_u32 s4, s4, s27
	s_addc_u32 s5, s5, 0
	global_load_dword v58, v5, s[4:5] nt
	s_add_u32 s4, s4, s27
	s_addc_u32 s5, s5, 0
	global_load_dword v59, v5, s[4:5] nt
	s_add_u32 s4, s4, s27
	s_addc_u32 s5, s5, 0
	global_load_dword v60, v5, s[4:5] nt
	s_add_u32 s4, s4, s27
	s_addc_u32 s5, s5, 0
	global_load_dword v61, v5, s[4:5] nt
	s_add_u32 s4, s4, s27
	s_addc_u32 s5, s5, 0
	global_load_dword v62, v5, s[4:5] nt
	s_add_u32 s4, s4, s27
	s_addc_u32 s5, s5, 0
	global_load_dword v63, v5, s[4:5] nt
	s_add_u32 s4, s4, s27
	s_addc_u32 s5, s5, 0
	global_load_dword v64, v5, s[4:5] nt
	s_add_u32 s4, s4, s27
	s_addc_u32 s5, s5, 0
	global_load_dword v65, v5, s[4:5] nt
	s_add_u32 s4, s4, s27
	s_addc_u32 s5, s5, 0
	global_load_dword v66, v5, s[4:5] nt
	s_add_u32 s4, s4, s27
	s_addc_u32 s5, s5, 0
	global_load_dword v67, v5, s[4:5] nt
	s_add_u32 s4, s4, s27
	s_addc_u32 s5, s5, 0
	global_load_dword v68, v5, s[4:5] nt
	s_add_u32 s4, s4, s27
	s_addc_u32 s5, s5, 0
	global_load_dword v69, v5, s[4:5] nt
	s_add_u32 s4, s4, s27
	s_addc_u32 s5, s5, 0
	global_load_dword v70, v5, s[4:5] nt
	s_add_u32 s4, s4, s27
	s_addc_u32 s5, s5, 0
	global_load_dword v71, v5, s[4:5] nt
	s_add_u32 s4, s4, s27
	s_addc_u32 s5, s5, 0
	s_waitcnt vmcnt(32)
	v_mul_f32_e32 v72, 0x42800000, v72
	v_mul_f32_e32 v73, 0x42800000, v73
	v_mul_f32_e32 v74, 0x42800000, v74
	v_mul_f32_e32 v75, 0x42800000, v75
	v_mul_f32_e32 v76, 0x42800000, v76
	v_mul_f32_e32 v77, 0x42800000, v77
	v_mul_f32_e32 v78, 0x42800000, v78
	v_mul_f32_e32 v79, 0x42800000, v79
	v_mul_f32_e32 v80, 0x42800000, v80
	v_mul_f32_e32 v81, 0x42800000, v81
	v_mul_f32_e32 v82, 0x42800000, v82
	v_mul_f32_e32 v83, 0x42800000, v83
	v_mul_f32_e32 v84, 0x42800000, v84
	v_mul_f32_e32 v85, 0x42800000, v85
	v_mul_f32_e32 v86, 0x42800000, v86
	v_mul_f32_e32 v87, 0x42800000, v87
	v_mul_f32_e32 v88, 0x42800000, v88
	v_mul_f32_e32 v89, 0x42800000, v89
	v_mul_f32_e32 v90, 0x42800000, v90
	v_mul_f32_e32 v91, 0x42800000, v91
	v_mul_f32_e32 v92, 0x42800000, v92
	v_mul_f32_e32 v93, 0x42800000, v93
	v_mul_f32_e32 v94, 0x42800000, v94
	v_mul_f32_e32 v95, 0x42800000, v95
	v_mul_f32_e32 v96, 0x42800000, v96
	v_mul_f32_e32 v97, 0x42800000, v97
	v_mul_f32_e32 v98, 0x42800000, v98
	v_mul_f32_e32 v99, 0x42800000, v99
	v_mul_f32_e32 v100, 0x42800000, v100
	v_mul_f32_e32 v101, 0x42800000, v101
	v_mul_f32_e32 v102, 0x42800000, v102
	v_mul_f32_e32 v103, 0x42800000, v103
	v_cvt_pk_fp8_f32 v112, v72, v73
	v_cvt_pk_fp8_f32 v112, v74, v75 op_sel:[0,0,1]
	v_cvt_pk_fp8_f32 v113, v76, v77
	v_cvt_pk_fp8_f32 v113, v78, v79 op_sel:[0,0,1]
	v_cvt_pk_fp8_f32 v114, v80, v81
	v_cvt_pk_fp8_f32 v114, v82, v83 op_sel:[0,0,1]
	v_cvt_pk_fp8_f32 v115, v84, v85
	v_cvt_pk_fp8_f32 v115, v86, v87 op_sel:[0,0,1]
	v_cvt_pk_fp8_f32 v116, v88, v89
	v_cvt_pk_fp8_f32 v116, v90, v91 op_sel:[0,0,1]
	v_cvt_pk_fp8_f32 v117, v92, v93
	v_cvt_pk_fp8_f32 v117, v94, v95 op_sel:[0,0,1]
	v_cvt_pk_fp8_f32 v118, v96, v97
	v_cvt_pk_fp8_f32 v118, v98, v99 op_sel:[0,0,1]
	v_cvt_pk_fp8_f32 v119, v100, v101
	v_cvt_pk_fp8_f32 v119, v102, v103 op_sel:[0,0,1]
	global_load_dword v72, v5, s[4:5] nt
	s_add_u32 s4, s4, s27
	s_addc_u32 s5, s5, 0
	global_load_dword v73, v5, s[4:5] nt
	s_add_u32 s4, s4, s27
	s_addc_u32 s5, s5, 0
	global_load_dword v74, v5, s[4:5] nt
	s_add_u32 s4, s4, s27
	s_addc_u32 s5, s5, 0
	global_load_dword v75, v5, s[4:5] nt
	s_add_u32 s4, s4, s27
	s_addc_u32 s5, s5, 0
	global_load_dword v76, v5, s[4:5] nt
	s_add_u32 s4, s4, s27
	s_addc_u32 s5, s5, 0
	global_load_dword v77, v5, s[4:5] nt
	s_add_u32 s4, s4, s27
	s_addc_u32 s5, s5, 0
	global_load_dword v78, v5, s[4:5] nt
	s_add_u32 s4, s4, s27
	s_addc_u32 s5, s5, 0
	global_load_dword v79, v5, s[4:5] nt
	s_add_u32 s4, s4, s27
	s_addc_u32 s5, s5, 0
	global_load_dword v80, v5, s[4:5] nt
	s_add_u32 s4, s4, s27
	s_addc_u32 s5, s5, 0
	global_load_dword v81, v5, s[4:5] nt
	s_add_u32 s4, s4, s27
	s_addc_u32 s5, s5, 0
	global_load_dword v82, v5, s[4:5] nt
	s_add_u32 s4, s4, s27
	s_addc_u32 s5, s5, 0
	global_load_dword v83, v5, s[4:5] nt
	s_add_u32 s4, s4, s27
	s_addc_u32 s5, s5, 0
	global_load_dword v84, v5, s[4:5] nt
	s_add_u32 s4, s4, s27
	s_addc_u32 s5, s5, 0
	global_load_dword v85, v5, s[4:5] nt
	s_add_u32 s4, s4, s27
	s_addc_u32 s5, s5, 0
	global_load_dword v86, v5, s[4:5] nt
	s_add_u32 s4, s4, s27
	s_addc_u32 s5, s5, 0
	global_load_dword v87, v5, s[4:5] nt
	s_add_u32 s4, s4, s27
	s_addc_u32 s5, s5, 0
	global_load_dword v88, v5, s[4:5] nt
	s_add_u32 s4, s4, s27
	s_addc_u32 s5, s5, 0
	global_load_dword v89, v5, s[4:5] nt
	s_add_u32 s4, s4, s27
	s_addc_u32 s5, s5, 0
	global_load_dword v90, v5, s[4:5] nt
	s_add_u32 s4, s4, s27
	s_addc_u32 s5, s5, 0
	global_load_dword v91, v5, s[4:5] nt
	s_add_u32 s4, s4, s27
	s_addc_u32 s5, s5, 0
	global_load_dword v92, v5, s[4:5] nt
	s_add_u32 s4, s4, s27
	s_addc_u32 s5, s5, 0
	global_load_dword v93, v5, s[4:5] nt
	s_add_u32 s4, s4, s27
	s_addc_u32 s5, s5, 0
	global_load_dword v94, v5, s[4:5] nt
	s_add_u32 s4, s4, s27
	s_addc_u32 s5, s5, 0
	global_load_dword v95, v5, s[4:5] nt
	s_add_u32 s4, s4, s27
	s_addc_u32 s5, s5, 0
	global_load_dword v96, v5, s[4:5] nt
	s_add_u32 s4, s4, s27
	s_addc_u32 s5, s5, 0
	global_load_dword v97, v5, s[4:5] nt
	s_add_u32 s4, s4, s27
	s_addc_u32 s5, s5, 0
	global_load_dword v98, v5, s[4:5] nt
	s_add_u32 s4, s4, s27
	s_addc_u32 s5, s5, 0
	global_load_dword v99, v5, s[4:5] nt
	s_add_u32 s4, s4, s27
	s_addc_u32 s5, s5, 0
	global_load_dword v100, v5, s[4:5] nt
	s_add_u32 s4, s4, s27
	s_addc_u32 s5, s5, 0
	global_load_dword v101, v5, s[4:5] nt
	s_add_u32 s4, s4, s27
	s_addc_u32 s5, s5, 0
	global_load_dword v102, v5, s[4:5] nt
	s_add_u32 s4, s4, s27
	s_addc_u32 s5, s5, 0
	global_load_dword v103, v5, s[4:5] nt
	s_add_u32 s4, s4, s27
	s_addc_u32 s5, s5, 0
	s_waitcnt vmcnt(32)
	v_mul_f32_e32 v40, 0x42800000, v40
	v_mul_f32_e32 v41, 0x42800000, v41
	v_mul_f32_e32 v42, 0x42800000, v42
	v_mul_f32_e32 v43, 0x42800000, v43
	v_mul_f32_e32 v44, 0x42800000, v44
	v_mul_f32_e32 v45, 0x42800000, v45
	v_mul_f32_e32 v46, 0x42800000, v46
	v_mul_f32_e32 v47, 0x42800000, v47
	v_mul_f32_e32 v48, 0x42800000, v48
	v_mul_f32_e32 v49, 0x42800000, v49
	v_mul_f32_e32 v50, 0x42800000, v50
	v_mul_f32_e32 v51, 0x42800000, v51
	v_mul_f32_e32 v52, 0x42800000, v52
	v_mul_f32_e32 v53, 0x42800000, v53
	v_mul_f32_e32 v54, 0x42800000, v54
	v_mul_f32_e32 v55, 0x42800000, v55
	v_mul_f32_e32 v56, 0x42800000, v56
	v_mul_f32_e32 v57, 0x42800000, v57
	v_mul_f32_e32 v58, 0x42800000, v58
	v_mul_f32_e32 v59, 0x42800000, v59
	v_mul_f32_e32 v60, 0x42800000, v60
	v_mul_f32_e32 v61, 0x42800000, v61
	v_mul_f32_e32 v62, 0x42800000, v62
	v_mul_f32_e32 v63, 0x42800000, v63
	v_mul_f32_e32 v64, 0x42800000, v64
	v_mul_f32_e32 v65, 0x42800000, v65
	v_mul_f32_e32 v66, 0x42800000, v66
	v_mul_f32_e32 v67, 0x42800000, v67
	v_mul_f32_e32 v68, 0x42800000, v68
	v_mul_f32_e32 v69, 0x42800000, v69
	v_mul_f32_e32 v70, 0x42800000, v70
	v_mul_f32_e32 v71, 0x42800000, v71
	v_cvt_pk_fp8_f32 v120, v40, v41
	v_cvt_pk_fp8_f32 v120, v42, v43 op_sel:[0,0,1]
	v_cvt_pk_fp8_f32 v121, v44, v45
	v_cvt_pk_fp8_f32 v121, v46, v47 op_sel:[0,0,1]
	v_cvt_pk_fp8_f32 v122, v48, v49
	v_cvt_pk_fp8_f32 v122, v50, v51 op_sel:[0,0,1]
	v_cvt_pk_fp8_f32 v123, v52, v53
	v_cvt_pk_fp8_f32 v123, v54, v55 op_sel:[0,0,1]
	v_cvt_pk_fp8_f32 v124, v56, v57
	v_cvt_pk_fp8_f32 v124, v58, v59 op_sel:[0,0,1]
	v_cvt_pk_fp8_f32 v125, v60, v61
	v_cvt_pk_fp8_f32 v125, v62, v63 op_sel:[0,0,1]
	v_cvt_pk_fp8_f32 v126, v64, v65
	v_cvt_pk_fp8_f32 v126, v66, v67 op_sel:[0,0,1]
	v_cvt_pk_fp8_f32 v127, v68, v69
	v_cvt_pk_fp8_f32 v127, v70, v71 op_sel:[0,0,1]
	s_waitcnt vmcnt(0)
	v_mul_f32_e32 v72, 0x42800000, v72
	v_mul_f32_e32 v73, 0x42800000, v73
	v_mul_f32_e32 v74, 0x42800000, v74
	v_mul_f32_e32 v75, 0x42800000, v75
	v_mul_f32_e32 v76, 0x42800000, v76
	v_mul_f32_e32 v77, 0x42800000, v77
	v_mul_f32_e32 v78, 0x42800000, v78
	v_mul_f32_e32 v79, 0x42800000, v79
	v_mul_f32_e32 v80, 0x42800000, v80
	v_mul_f32_e32 v81, 0x42800000, v81
	v_mul_f32_e32 v82, 0x42800000, v82
	v_mul_f32_e32 v83, 0x42800000, v83
	v_mul_f32_e32 v84, 0x42800000, v84
	v_mul_f32_e32 v85, 0x42800000, v85
	v_mul_f32_e32 v86, 0x42800000, v86
	v_mul_f32_e32 v87, 0x42800000, v87
	v_mul_f32_e32 v88, 0x42800000, v88
	v_mul_f32_e32 v89, 0x42800000, v89
	v_mul_f32_e32 v90, 0x42800000, v90
	v_mul_f32_e32 v91, 0x42800000, v91
	v_mul_f32_e32 v92, 0x42800000, v92
	v_mul_f32_e32 v93, 0x42800000, v93
	v_mul_f32_e32 v94, 0x42800000, v94
	v_mul_f32_e32 v95, 0x42800000, v95
	v_mul_f32_e32 v96, 0x42800000, v96
	v_mul_f32_e32 v97, 0x42800000, v97
	v_mul_f32_e32 v98, 0x42800000, v98
	v_mul_f32_e32 v99, 0x42800000, v99
	v_mul_f32_e32 v100, 0x42800000, v100
	v_mul_f32_e32 v101, 0x42800000, v101
	v_mul_f32_e32 v102, 0x42800000, v102
	v_mul_f32_e32 v103, 0x42800000, v103
	v_cvt_pk_fp8_f32 v128, v72, v73
	v_cvt_pk_fp8_f32 v128, v74, v75 op_sel:[0,0,1]
	v_cvt_pk_fp8_f32 v129, v76, v77
	v_cvt_pk_fp8_f32 v129, v78, v79 op_sel:[0,0,1]
	v_cvt_pk_fp8_f32 v130, v80, v81
	v_cvt_pk_fp8_f32 v130, v82, v83 op_sel:[0,0,1]
	v_cvt_pk_fp8_f32 v131, v84, v85
	v_cvt_pk_fp8_f32 v131, v86, v87 op_sel:[0,0,1]
	v_cvt_pk_fp8_f32 v132, v88, v89
	v_cvt_pk_fp8_f32 v132, v90, v91 op_sel:[0,0,1]
	v_cvt_pk_fp8_f32 v133, v92, v93
	v_cvt_pk_fp8_f32 v133, v94, v95 op_sel:[0,0,1]
	v_cvt_pk_fp8_f32 v134, v96, v97
	v_cvt_pk_fp8_f32 v134, v98, v99 op_sel:[0,0,1]
	v_cvt_pk_fp8_f32 v135, v100, v101
	v_cvt_pk_fp8_f32 v135, v102, v103 op_sel:[0,0,1]
	s_nop 4
	ds_write_b128 v12, v[104:107]
	ds_write_b128 v12, v[108:111] offset:16
	ds_write_b128 v12, v[112:115] offset:32
	ds_write_b128 v12, v[116:119] offset:48
	ds_write_b128 v12, v[120:123] offset:64
	ds_write_b128 v12, v[124:127] offset:80
	ds_write_b128 v12, v[128:131] offset:96
	ds_write_b128 v12, v[132:135] offset:112
	ds_read_b128 v[40:43], v13
	ds_read_b128 v[44:47], v13 offset:1152
	ds_read_b128 v[48:51], v13 offset:2304
	ds_read_b128 v[52:55], v13 offset:3456
	ds_read_b128 v[56:59], v13 offset:4608
	ds_read_b128 v[60:63], v13 offset:5760
	ds_read_b128 v[64:67], v13 offset:6912
	ds_read_b128 v[68:71], v13 offset:8064
	s_waitcnt lgkmcnt(7)
	global_store_dwordx4 v6, v[40:43], s[10:11]
	v_add_u32_e32 v6, s32, v6
	s_waitcnt lgkmcnt(6)
	global_store_dwordx4 v6, v[44:47], s[10:11]
	v_add_u32_e32 v6, s32, v6
	s_waitcnt lgkmcnt(5)
	global_store_dwordx4 v6, v[48:51], s[10:11]
	v_add_u32_e32 v6, s32, v6
	s_waitcnt lgkmcnt(4)
	global_store_dwordx4 v6, v[52:55], s[10:11]
	v_add_u32_e32 v6, s32, v6
	s_waitcnt lgkmcnt(3)
	global_store_dwordx4 v6, v[56:59], s[10:11]
	v_add_u32_e32 v6, s32, v6
	s_waitcnt lgkmcnt(2)
	global_store_dwordx4 v6, v[60:63], s[10:11]
	v_add_u32_e32 v6, s32, v6
	s_waitcnt lgkmcnt(1)
	global_store_dwordx4 v6, v[64:67], s[10:11]
	v_add_u32_e32 v6, s32, v6
	s_waitcnt lgkmcnt(0)
	global_store_dwordx4 v6, v[68:71], s[10:11]
.Lcv_next:
	s_add_i32 s22, s22, 1
	s_cmp_lt_u32 s22, 21
	s_cbranch_scc1 .Lcv_unit
	s_waitcnt vmcnt(0) lgkmcnt(0)
	s_barrier
	s_branch .Lcv_ret
